# bundle9 + attention loop trims: 32-bit saddr K/V prefetch addressing (-15 VALU), packed output scaling (-12), no self-max canonicalisation (-5)
# speedup vs baseline: 1.0063x; 1.0063x over previous
.LBB0_412:
	s_mul_hi_i32 s23, s39, 0x2aaaaaab
	s_lshr_b32 s24, s23, 31
	s_ashr_i32 s23, s23, 5
	s_add_i32 s34, s23, s24
	s_mul_i32 s23, s34, 0xffffff40
	s_add_i32 s23, s39, s23
	s_mov_b32 s31, s25
	s_and_b32 s49, s38, 1
	s_ashr_i32 s24, s23, 6
	s_and_b32 s25, s39, 63
	s_ashr_i32 s36, s34, 4
	s_cmp_eq_u32 s24, 1
	s_cselect_b64 s[26:27], -1, 0
	s_and_b64 s[28:29], s[26:27], exec
	s_cselect_b32 s35, 3, 15
	s_cselect_b32 s37, 2, 4
	s_cmp_lt_u32 s23, 64
	s_cselect_b64 s[28:29], -1, 0
	s_and_b64 s[56:57], s[28:29], exec
	s_cselect_b32 s62, 0, s37
	s_waitcnt vmcnt(2)
	v_mov_b64_e32 v[88:89], v[10:11]
	s_cselect_b32 s23, 0, s35
	s_lshr_b32 s25, s25, s62
	s_waitcnt vmcnt(1)
	v_mov_b64_e32 v[50:51], v[14:15]
	v_mov_b64_e32 v[86:87], v[8:9]
	v_sub_u32_e64 v8, s25, 1 clamp
	v_mov_b64_e32 v[48:49], v[12:13]
	s_ashr_i32 s35, s34, 31
	v_lshlrev_b32_e32 v12, 7, v8
	s_and_b32 s23, s23, s70
	s_lshl_b64 s[56:57], s[34:35], 13
	s_or_b32 s56, s56, s23
	v_mov_b32_e32 v204, s56
	v_or_b32_e32 v8, v12, v172
	v_lshl_add_u32 v8, v8, s62, v204
	v_lshl_or_b32 v8, v8, 7, v191
	global_load_dwordx4 v[16:19], v8, s[76:77]
	global_load_dwordx4 v[20:23], v8, s[78:79]
	v_or_b32_e32 v8, v12, v174
	v_lshl_add_u32 v8, v8, s62, v204
	v_lshl_or_b32 v8, v8, 7, v191
	s_lshl_b32 s63, s25, 7
	global_load_dwordx4 v[24:27], v8, s[76:77]
	global_load_dwordx4 v[28:31], v8, s[78:79]
	v_or_b32_e32 v8, s63, v172
	v_lshl_add_u32 v8, v8, s62, v204
	v_lshl_or_b32 v8, v8, 7, v191
	global_load_dwordx4 v[32:35], v8, s[76:77]
	global_load_dwordx4 v[36:39], v8, s[78:79]
	v_or_b32_e32 v8, s63, v175
	v_lshl_add_u32 v8, v8, s62, v204
	v_lshl_or_b32 v8, v8, 7, v191
	global_load_dwordx4 v[40:43], v8, s[76:77]
	global_load_dwordx4 v[44:47], v8, s[78:79]
	s_ashr_i32 s37, s36, 31
	v_add_u32_e32 v8, s63, v181
	s_lshl_b64 s[36:37], s[36:37], 13
	v_ashrrev_i32_e32 v9, 31, v8
	s_or_b32 s36, s36, s23
	v_lshlrev_b64 v[8:9], s62, v[8:9]
	v_lshl_add_u64 v[164:165], s[36:37], 0, v[8:9]
	v_lshlrev_b64 v[162:163], 6, v[164:165]
	s_lshl_b64 s[36:37], s[34:35], 20
	s_add_u32 s36, s64, s36
	v_lshlrev_b32_e32 v8, 1, v162
	s_addc_u32 s37, s65, s37
	v_and_b32_e32 v64, 0xfff80, v8
	v_lshl_add_u64 v[8:9], s[36:37], 0, v[64:65]
	v_mov_b32_e32 v169, v65
	v_lshl_add_u64 v[12:13], v[8:9], 0, v[168:169]
	global_load_dwordx4 v[8:11], v[12:13], off
	s_nop 0
	global_load_dwordx4 v[12:15], v[12:13], off offset:64
	s_mul_i32 s23, s49, 0x12000
	s_add_i32 s23, s23, 0
	v_add3_u32 v56, s23, v182, v215
	v_add3_u32 v64, s23, v183, v215
	ds_read_b128 v[52:55], v56
	ds_read_b128 v[56:59], v56 offset:64
	ds_read_b128 v[60:63], v64
	ds_read_b128 v[66:69], v64 offset:64
	v_add3_u32 v64, s23, v184, v215
	ds_read_b128 v[70:73], v64
	ds_read_b128 v[74:77], v64 offset:64
	v_add3_u32 v64, s23, v185, v215
	ds_read_b128 v[90:93], v64
	ds_read_b128 v[94:97], v64 offset:64
	v_add3_u32 v64, s23, v186, v215
	ds_read_b128 v[98:101], v64
	ds_read_b128 v[102:105], v64 offset:64
	v_add3_u32 v64, s23, v187, v215
	ds_read_b128 v[106:109], v64
	ds_read_b128 v[110:113], v64 offset:64
	v_add3_u32 v64, s23, v188, v215
	ds_read_b128 v[114:117], v64
	ds_read_b128 v[118:121], v64 offset:64
	v_add3_u32 v64, s23, v189, v215
	ds_read_b128 v[122:125], v64
	ds_read_b128 v[126:129], v64 offset:64
	v_add3_u32 v64, s23, v190, v215
	ds_read_b128 v[130:133], v64
	ds_read_b128 v[134:137], v64 offset:64
	s_waitcnt lgkmcnt(14)
	v_mfma_f32_16x16x32_bf16 v[52:55], v[52:55], v[86:89], v[4:7]
	s_cmp_lg_u32 s31, 0
	v_mfma_f32_16x16x32_bf16 v[82:85], v[56:59], v[48:51], v[52:55]
	v_mfma_f32_16x16x32_bf16 v[52:55], v[60:63], v[86:89], 0
	v_mfma_f32_16x16x32_bf16 v[78:81], v[66:69], v[48:51], v[52:55]
	s_waitcnt lgkmcnt(13)
	v_mfma_f32_16x16x32_bf16 v[52:55], v[70:73], v[86:89], 0
	s_waitcnt lgkmcnt(12)
	v_mfma_f32_16x16x32_bf16 v[74:77], v[74:77], v[48:51], v[52:55]
	s_waitcnt lgkmcnt(11)
	v_mfma_f32_16x16x32_bf16 v[52:55], v[90:93], v[86:89], 0
	s_waitcnt lgkmcnt(10)
	v_mfma_f32_16x16x32_bf16 v[70:73], v[94:97], v[48:51], v[52:55]
	s_waitcnt lgkmcnt(9)
	v_mfma_f32_16x16x32_bf16 v[52:55], v[98:101], v[86:89], 0
	s_waitcnt lgkmcnt(8)
	v_mfma_f32_16x16x32_bf16 v[66:69], v[102:105], v[48:51], v[52:55]
	s_waitcnt lgkmcnt(7)
	v_mfma_f32_16x16x32_bf16 v[52:55], v[106:109], v[86:89], 0
	s_waitcnt lgkmcnt(6)
	v_mfma_f32_16x16x32_bf16 v[60:63], v[110:113], v[48:51], v[52:55]
	s_waitcnt lgkmcnt(5)
	v_mfma_f32_16x16x32_bf16 v[52:55], v[114:117], v[86:89], 0
	s_waitcnt lgkmcnt(4)
	v_mfma_f32_16x16x32_bf16 v[56:59], v[118:121], v[48:51], v[52:55]
	s_waitcnt lgkmcnt(3)
	v_mfma_f32_16x16x32_bf16 v[52:55], v[122:125], v[86:89], 0
	s_waitcnt lgkmcnt(1)
	v_mfma_f32_16x16x32_bf16 v[86:89], v[130:133], v[86:89], v[0:3]
	v_mfma_f32_16x16x32_bf16 v[52:55], v[126:129], v[48:51], v[52:55]
	s_waitcnt lgkmcnt(0)
	v_mfma_f32_16x16x32_bf16 v[48:51], v[134:137], v[48:51], v[86:89]
	s_cbranch_scc1 .LBB0_414
	s_nop 3
	v_pk_add_f32 v[86:87], v[84:85], s[84:85] op_sel_hi:[1,0]
	v_pk_add_f32 v[88:89], v[82:83], s[84:85] op_sel_hi:[1,0]
	v_cndmask_b32_e64 v85, v85, v87, s[20:21]
	v_cndmask_b32_e64 v84, v84, v86, s[20:21]
	v_cndmask_b32_e64 v83, v83, v89, s[20:21]
	v_cndmask_b32_e64 v82, v82, v88, s[20:21]
	v_pk_add_f32 v[86:87], v[80:81], s[84:85] op_sel_hi:[1,0]
	v_pk_add_f32 v[88:89], v[78:79], s[84:85] op_sel_hi:[1,0]
	v_cndmask_b32_e64 v81, v81, v87, s[18:19]
	v_cndmask_b32_e64 v80, v80, v86, s[18:19]
	v_cndmask_b32_e64 v79, v79, v89, s[18:19]
	v_cndmask_b32_e64 v78, v78, v88, s[18:19]
	v_pk_add_f32 v[86:87], v[76:77], s[84:85] op_sel_hi:[1,0]
	v_pk_add_f32 v[88:89], v[74:75], s[84:85] op_sel_hi:[1,0]
	v_cndmask_b32_e64 v77, v77, v87, s[16:17]
	v_cndmask_b32_e64 v76, v76, v86, s[16:17]
	v_cndmask_b32_e64 v75, v75, v89, s[16:17]
	v_cndmask_b32_e64 v74, v74, v88, s[16:17]
	v_pk_add_f32 v[86:87], v[72:73], s[84:85] op_sel_hi:[1,0]
	v_pk_add_f32 v[88:89], v[70:71], s[84:85] op_sel_hi:[1,0]
	v_cndmask_b32_e64 v73, v73, v87, s[14:15]
	v_cndmask_b32_e64 v72, v72, v86, s[14:15]
	v_cndmask_b32_e64 v71, v71, v89, s[14:15]
	v_cndmask_b32_e64 v70, v70, v88, s[14:15]
	v_pk_add_f32 v[86:87], v[68:69], s[84:85] op_sel_hi:[1,0]
	v_pk_add_f32 v[88:89], v[66:67], s[84:85] op_sel_hi:[1,0]
	v_cndmask_b32_e64 v69, v69, v87, s[12:13]
	v_cndmask_b32_e64 v68, v68, v86, s[12:13]
	v_cndmask_b32_e64 v67, v67, v89, s[12:13]
	v_cndmask_b32_e64 v66, v66, v88, s[12:13]
	v_pk_add_f32 v[86:87], v[62:63], s[84:85] op_sel_hi:[1,0]
	v_pk_add_f32 v[88:89], v[60:61], s[84:85] op_sel_hi:[1,0]
	v_cndmask_b32_e64 v63, v63, v87, s[10:11]
	v_cndmask_b32_e64 v62, v62, v86, s[10:11]
	v_cndmask_b32_e64 v61, v61, v89, s[10:11]
	v_cndmask_b32_e64 v60, v60, v88, s[10:11]
	v_pk_add_f32 v[86:87], v[58:59], s[84:85] op_sel_hi:[1,0]
	v_pk_add_f32 v[88:89], v[56:57], s[84:85] op_sel_hi:[1,0]
	v_cndmask_b32_e64 v59, v59, v87, s[8:9]
	v_cndmask_b32_e64 v58, v58, v86, s[8:9]
	v_cndmask_b32_e64 v57, v57, v89, s[8:9]
	v_cndmask_b32_e64 v56, v56, v88, s[8:9]
	v_pk_add_f32 v[86:87], v[54:55], s[84:85] op_sel_hi:[1,0]
	v_pk_add_f32 v[88:89], v[52:53], s[84:85] op_sel_hi:[1,0]
	v_cndmask_b32_e64 v55, v55, v87, s[6:7]
	v_cndmask_b32_e64 v54, v54, v86, s[6:7]
	v_cndmask_b32_e64 v53, v53, v89, s[6:7]
	v_cndmask_b32_e64 v52, v52, v88, s[6:7]
.LBB0_414:
	v_add3_u32 v64, s23, v173, v171
	ds_read_b64_tr_b16 v[90:91], v64 offset:36864
	s_nop 1
	ds_read_b64_tr_b16 v[86:87], v64 offset:36896
	ds_read_b64_tr_b16 v[100:101], v64 offset:36928
	ds_read_b64_tr_b16 v[108:109], v64 offset:36960
	ds_read_b64_tr_b16 v[92:93], v64 offset:39168
	ds_read_b64_tr_b16 v[88:89], v64 offset:39200
	ds_read_b64_tr_b16 v[102:103], v64 offset:39232
	ds_read_b64_tr_b16 v[110:111], v64 offset:39264
	ds_read_b64_tr_b16 v[104:105], v64 offset:41472
	ds_read_b64_tr_b16 v[112:113], v64 offset:41504
	ds_read_b64_tr_b16 v[118:119], v64 offset:41536
	ds_read_b64_tr_b16 v[126:127], v64 offset:41568
	ds_read_b64_tr_b16 v[106:107], v64 offset:43776
	ds_read_b64_tr_b16 v[114:115], v64 offset:43808
	ds_read_b64_tr_b16 v[120:121], v64 offset:43840
	ds_read_b64_tr_b16 v[128:129], v64 offset:43872
	ds_read_b64_tr_b16 v[122:123], v64 offset:46080
	ds_read_b64_tr_b16 v[130:131], v64 offset:46112
	ds_read_b64_tr_b16 v[138:139], v64 offset:46144
	ds_read_b64_tr_b16 v[146:147], v64 offset:46176
	ds_read_b64_tr_b16 v[124:125], v64 offset:48384
	ds_read_b64_tr_b16 v[132:133], v64 offset:48416
	ds_read_b64_tr_b16 v[140:141], v64 offset:48448
	ds_read_b64_tr_b16 v[148:149], v64 offset:48480
	ds_read_b64_tr_b16 v[142:143], v64 offset:50688
	ds_read_b64_tr_b16 v[152:153], v64 offset:50720
	ds_read_b64_tr_b16 v[156:157], v64 offset:50752
	ds_read_b64_tr_b16 v[134:135], v64 offset:50784
	ds_read_b64_tr_b16 v[144:145], v64 offset:52992
	ds_read_b64_tr_b16 v[154:155], v64 offset:53024
	ds_read_b64_tr_b16 v[158:159], v64 offset:53056
	ds_read_b64_tr_b16 v[136:137], v64 offset:53088
	ds_read_b64_tr_b16 v[150:151], v64 offset:55296
	ds_read_b64_tr_b16 v[116:117], v64 offset:55328
	ds_read_b64_tr_b16 v[98:99], v64 offset:55360
	ds_read_b64_tr_b16 v[94:95], v64 offset:55392
	v_max3_f32 v64, v82, s84, v83
	v_max3_f32 v64, v64, v84, v85
	v_max3_f32 v64, v64, v78, v79
	v_max3_f32 v64, v64, v80, v81
	v_max3_f32 v64, v64, v74, v75
	v_max3_f32 v64, v64, v76, v77
	v_max3_f32 v64, v64, v70, v71
	v_max3_f32 v64, v64, v72, v73
	v_max3_f32 v64, v64, v66, v67
	v_max3_f32 v64, v64, v68, v69
	v_max3_f32 v64, v64, v60, v61
	v_max3_f32 v64, v64, v62, v63
	v_max3_f32 v64, v64, v56, v57
	v_max3_f32 v64, v64, v58, v59
	v_max3_f32 v64, v64, v52, v53
	v_max3_f32 v64, v64, v54, v55
	v_max3_f32 v64, v64, v48, v49
	v_max3_f32 v64, v64, v50, v51
	v_mov_b32_e32 v96, v64
	s_nop 1
	v_permlane16_swap_b32_e32 v64, v96
	v_max_f32_e32 v64, v64, v96
	v_mov_b32_e32 v96, v64
	s_nop 1
	v_permlane32_swap_b32_e32 v64, v96
	v_max_f32_e32 v170, v64, v96
	v_pk_add_f32 v[82:83], v[82:83], v[170:171] op_sel_hi:[1,0] neg_lo:[0,1] neg_hi:[0,1]
	v_pk_add_f32 v[84:85], v[84:85], v[170:171] op_sel_hi:[1,0] neg_lo:[0,1] neg_hi:[0,1]
	v_exp_f32_e32 v82, v82
	v_exp_f32_e32 v83, v83
	v_exp_f32_e32 v84, v84
	v_exp_f32_e32 v85, v85
	v_pk_add_f32 v[78:79], v[78:79], v[170:171] op_sel_hi:[1,0] neg_lo:[0,1] neg_hi:[0,1]
	v_pk_add_f32 v[80:81], v[80:81], v[170:171] op_sel_hi:[1,0] neg_lo:[0,1] neg_hi:[0,1]
	v_exp_f32_e32 v78, v78
	v_exp_f32_e32 v79, v79
	v_exp_f32_e32 v80, v80
	v_exp_f32_e32 v81, v81
	v_pk_add_f32 v[74:75], v[74:75], v[170:171] op_sel_hi:[1,0] neg_lo:[0,1] neg_hi:[0,1]
	v_pk_add_f32 v[76:77], v[76:77], v[170:171] op_sel_hi:[1,0] neg_lo:[0,1] neg_hi:[0,1]
	v_exp_f32_e32 v192, v74
	v_exp_f32_e32 v193, v75
	v_pk_add_f32 v[96:97], v[84:85], v[82:83]
	v_exp_f32_e32 v194, v76
	v_exp_f32_e32 v195, v77
	v_pk_add_f32 v[70:71], v[70:71], v[170:171] op_sel_hi:[1,0] neg_lo:[0,1] neg_hi:[0,1]
	v_pk_add_f32 v[74:75], v[78:79], v[96:97]
	v_pk_add_f32 v[72:73], v[72:73], v[170:171] op_sel_hi:[1,0] neg_lo:[0,1] neg_hi:[0,1]
	v_exp_f32_e32 v96, v70
	v_exp_f32_e32 v97, v71
	v_pk_add_f32 v[74:75], v[80:81], v[74:75]
	v_exp_f32_e32 v196, v72
	v_exp_f32_e32 v197, v73
	v_pk_add_f32 v[66:67], v[66:67], v[170:171] op_sel_hi:[1,0] neg_lo:[0,1] neg_hi:[0,1]
	v_pk_add_f32 v[74:75], v[192:193], v[74:75]
	v_pk_add_f32 v[68:69], v[68:69], v[170:171] op_sel_hi:[1,0] neg_lo:[0,1] neg_hi:[0,1]
	v_exp_f32_e32 v198, v66
	v_exp_f32_e32 v199, v67
	v_pk_add_f32 v[74:75], v[194:195], v[74:75]
	v_exp_f32_e32 v200, v68
	v_exp_f32_e32 v201, v69
	v_pk_add_f32 v[66:67], v[96:97], v[74:75]
	v_cvt_pk_bf16_f32 v68, v78, v79
	v_pk_add_f32 v[66:67], v[196:197], v[66:67]
	v_cvt_pk_bf16_f32 v69, v80, v81
	v_pk_add_f32 v[66:67], v[198:199], v[66:67]
	v_pk_add_f32 v[74:75], v[60:61], v[170:171] op_sel_hi:[1,0] neg_lo:[0,1] neg_hi:[0,1]
	v_pk_add_f32 v[202:203], v[200:201], v[66:67]
	v_cvt_pk_bf16_f32 v66, v82, v83
	v_cvt_pk_bf16_f32 v67, v84, v85
	v_pk_add_f32 v[76:77], v[62:63], v[170:171] op_sel_hi:[1,0] neg_lo:[0,1] neg_hi:[0,1]
	v_exp_f32_e32 v78, v74
	s_waitcnt lgkmcnt(14)
	v_mfma_f32_16x16x32_bf16 v[70:73], v[90:93], v[66:69], 0
	v_exp_f32_e32 v79, v75
	v_exp_f32_e32 v80, v76
	v_exp_f32_e32 v81, v77
	v_mfma_f32_16x16x32_bf16 v[60:63], v[86:89], v[66:69], 0
	v_add_f32_e64 v84, v56, -v170
	v_add_f32_e64 v85, v57, -v170
	v_pk_add_f32 v[86:87], v[58:59], v[170:171] op_sel_hi:[1,0] neg_lo:[0,1] neg_hi:[0,1]
	v_exp_f32_e32 v84, v84
	v_mfma_f32_16x16x32_bf16 v[74:77], v[100:103], v[66:69], 0
	v_exp_f32_e32 v85, v85
	v_exp_f32_e32 v86, v86
	v_exp_f32_e32 v87, v87
	v_mfma_f32_16x16x32_bf16 v[56:59], v[108:111], v[66:69], 0
	v_cvt_pk_bf16_f32 v66, v192, v193
	v_cvt_pk_bf16_f32 v67, v194, v195
	v_cvt_pk_bf16_f32 v68, v96, v97
	v_cvt_pk_bf16_f32 v69, v196, v197
	v_pk_add_f32 v[88:89], v[52:53], v[170:171] op_sel_hi:[1,0] neg_lo:[0,1] neg_hi:[0,1]
	v_pk_add_f32 v[82:83], v[78:79], v[202:203]
	v_mfma_f32_16x16x32_bf16 v[70:73], v[104:107], v[66:69], v[70:73]
	v_add_f32_e64 v90, v54, -v170
	v_add_f32_e64 v91, v55, -v170
	v_pk_add_f32 v[82:83], v[80:81], v[82:83]
	v_pk_add_f32 v[48:49], v[48:49], v[170:171] op_sel_hi:[1,0] neg_lo:[0,1] neg_hi:[0,1]
	v_mfma_f32_16x16x32_bf16 v[60:63], v[112:115], v[66:69], v[60:63]
	v_add_f32_e64 v82, v84, v82
	v_add_f32_e64 v83, v85, v83
	s_waitcnt lgkmcnt(1)
	v_mov_b32_e32 v100, v98
	v_pk_add_f32 v[82:83], v[86:87], v[82:83]
	v_mfma_f32_16x16x32_bf16 v[74:77], v[118:121], v[66:69], v[74:77]
	v_mov_b32_e32 v118, v116
	v_mov_b32_e32 v119, v117
	v_mov_b32_e32 v101, v99
	v_mfma_f32_16x16x32_bf16 v[52:55], v[126:129], v[66:69], v[56:59]
	s_waitcnt lgkmcnt(0)
	v_mov_b32_e32 v96, v94
	v_mov_b32_e32 v97, v95
	v_mov_b32_e32 v64, v65
	v_cvt_pk_bf16_f32 v58, v78, v79
	v_exp_f32_e32 v78, v88
	v_exp_f32_e32 v79, v89
	v_cvt_pk_bf16_f32 v56, v198, v199
	v_cvt_pk_bf16_f32 v57, v200, v201
	v_cvt_pk_bf16_f32 v59, v80, v81
	v_exp_f32_e32 v80, v90
	v_exp_f32_e32 v81, v91
	v_mfma_f32_16x16x32_bf16 v[66:69], v[122:125], v[56:59], v[70:73]
	v_add_f32_e64 v82, v78, v82
	v_add_f32_e64 v83, v79, v83
	s_cmp_eq_u32 s30, 1
	s_mov_b32 s23, 0xe800000
	v_mfma_f32_16x16x32_bf16 v[60:63], v[130:133], v[56:59], v[60:63]
	s_cselect_b32 s23, s23, 0x2e800000
	s_cmp_lg_u32 s30, 0
	s_cselect_b32 s23, s23, 0x12800000
	v_mfma_f32_16x16x32_bf16 v[70:73], v[138:141], v[56:59], v[74:77]
	s_add_u32 s36, s42, s23
	s_addc_u32 s37, s43, 0
	s_lshl_b32 s66, s22, 6
	v_pk_add_f32 v[74:75], v[50:51], v[170:171] op_sel_hi:[1,0] neg_lo:[0,1] neg_hi:[0,1]
	v_exp_f32_e32 v76, v48
	v_exp_f32_e32 v77, v49
	v_exp_f32_e32 v74, v74
	v_exp_f32_e32 v75, v75
	v_mfma_f32_16x16x32_bf16 v[48:51], v[146:149], v[56:59], v[52:55]
	s_nop 2
	v_cvt_pk_bf16_f32 v52, v84, v85
	v_cvt_pk_bf16_f32 v53, v86, v87
	v_cvt_pk_bf16_f32 v54, v78, v79
	v_cvt_pk_bf16_f32 v55, v80, v81
	v_pk_add_f32 v[78:79], v[80:81], v[82:83]
	s_nop 0
	v_mfma_f32_16x16x32_bf16 v[56:59], v[142:145], v[52:55], v[66:69]
	v_mfma_f32_16x16x32_bf16 v[66:69], v[152:155], v[52:55], v[60:63]
	v_mov_b32_e32 v152, v150
	v_mov_b32_e32 v153, v151
	s_nop 0
	v_pk_add_f32 v[60:61], v[76:77], v[78:79]
	v_mfma_f32_16x16x32_bf16 v[70:73], v[156:159], v[52:55], v[70:73]
	v_add_f32_e64 v60, v74, v60
	v_add_f32_e64 v61, v75, v61
	v_cvt_pk_bf16_f32 v62, v76, v77
	v_pk_add_f32 v[60:61], v[60:61], v[60:61] op_sel:[0,1] op_sel_hi:[1,0]
	v_mfma_f32_16x16x32_bf16 v[48:51], v[134:137], v[52:55], v[48:51]
	v_mov_b32_e32 v61, v60
	s_nop 1
	v_permlane16_swap_b32_e32 v60, v61
	v_cvt_pk_bf16_f32 v63, v74, v75
	v_add_f32_e32 v74, v60, v61
	s_nop 0
	v_mfma_f32_16x16x32_bf16 v[52:55], v[150:153], v[62:65], v[56:59]
	v_mfma_f32_16x16x32_bf16 v[56:59], v[116:119], v[62:65], v[66:69]
	v_mfma_f32_16x16x32_bf16 v[66:69], v[98:101], v[62:65], v[70:73]
	s_nop 2
	v_mov_b32_e32 v70, v74
	s_nop 1
	v_permlane32_swap_b32_e32 v74, v70
	v_mfma_f32_16x16x32_bf16 v[60:63], v[94:97], v[62:65], v[48:51]
	s_nop 2
	v_add_f32_e32 v48, v74, v70
	v_rcp_f32_e32 v49, v48
	s_nop 0
	v_mul_f32_e32 v206, 0x42800000, v49
	v_pk_mul_f32 v[208:209], v[52:53], v[206:207] op_sel_hi:[1,0]
	v_pk_mul_f32 v[210:211], v[54:55], v[206:207] op_sel_hi:[1,0]
	v_pk_mul_f32 v[212:213], v[56:57], v[206:207] op_sel_hi:[1,0]
	v_pk_mul_f32 v[216:217], v[58:59], v[206:207] op_sel_hi:[1,0]
	v_pk_mul_f32 v[218:219], v[66:67], v[206:207] op_sel_hi:[1,0]
	v_pk_mul_f32 v[220:221], v[68:69], v[206:207] op_sel_hi:[1,0]
	v_pk_mul_f32 v[222:223], v[60:61], v[206:207] op_sel_hi:[1,0]
	v_pk_mul_f32 v[224:225], v[62:63], v[206:207] op_sel_hi:[1,0]
	v_med3_f32 v208, v208, s55, v228
	v_med3_f32 v209, v209, s55, v228
	v_med3_f32 v210, v210, s55, v228
	v_med3_f32 v211, v211, s55, v228
	v_med3_f32 v212, v212, s55, v228
	v_med3_f32 v213, v213, s55, v228
	v_med3_f32 v216, v216, s55, v228
	v_med3_f32 v217, v217, s55, v228
	v_med3_f32 v218, v218, s55, v228
	v_med3_f32 v219, v219, s55, v228
	v_med3_f32 v220, v220, s55, v228
	v_med3_f32 v221, v221, s55, v228
	v_med3_f32 v222, v222, s55, v228
	v_med3_f32 v223, v223, s55, v228
	v_med3_f32 v224, v224, s55, v228
	v_med3_f32 v225, v225, s55, v228
	v_cvt_pk_fp8_f32 v50, v208, v209
	v_cvt_pk_fp8_f32 v50, v210, v211 op_sel:[0,0,1]
	v_cvt_pk_fp8_f32 v51, v212, v213
	v_cvt_pk_fp8_f32 v51, v216, v217 op_sel:[0,0,1]
	v_cvt_pk_fp8_f32 v52, v218, v219
	v_cvt_pk_fp8_f32 v52, v220, v221 op_sel:[0,0,1]
	v_cvt_pk_fp8_f32 v53, v222, v223
	v_cvt_pk_fp8_f32 v53, v224, v225 op_sel:[0,0,1]
	v_lshlrev_b64 v[54:55], 10, v[166:167]
	v_lshl_add_u64 v[54:55], s[36:37], 0, v[54:55]
	v_lshl_add_u64 v[54:55], v[54:55], 0, s[66:67]
	v_lshl_add_u64 v[54:55], v[54:55], 0, v[160:161]
	global_store_dwordx4 v[54:55], v[50:53], off
	s_and_saveexec_b64 s[36:37], vcc
	s_cbranch_execz .LBB0_416
	v_log_f32_e32 v48, v48
	s_ashr_i32 s31, s30, 31
	s_lshl_b64 s[30:31], s[30:31], 22
	v_readlane_b32 s23, v254, 30
	s_add_u32 s30, s23, s30
	v_readlane_b32 s23, v254, 31
	v_add_f32_e32 v48, v170, v48
	s_addc_u32 s31, s23, s31
	v_mul_f32_e32 v50, 0x3f317218, v48
	v_lshlrev_b64 v[48:49], 6, v[166:167]
	v_lshl_add_u64 v[48:49], s[30:31], 0, v[48:49]
	s_mov_b32 s23, s67
	v_lshl_add_u64 v[48:49], s[22:23], 2, v[48:49]
	global_store_dword v[48:49], v50, off
